# fp8 GEMM loops: every MFMA burst starts on an 8-byte boundary (one s_nop 0 in front of the misaligned ones)
# baseline (speedup 1.0000x reference)
.LBB0_824:
	s_add_u32 s34, s26, 0xf2fc0080
	s_addc_u32 s35, s27, -1
	s_and_b64 s[30:31], s[28:29], exec
	s_cselect_b32 s31, 0, s34
	s_cselect_b32 s30, 0, s35
	s_add_u32 s34, s14, s31
	s_addc_u32 s35, s15, s30
	s_and_b64 s[28:29], s[28:29], exec
	s_waitcnt lgkmcnt(8)
	s_barrier
	s_waitcnt lgkmcnt(0)
	s_cselect_b32 s28, s20, s11
	s_cselect_b32 s29, s21, s23
	s_add_u32 s30, s28, 0x4000
	s_addc_u32 s31, s29, 0
	s_setprio 1
	s_waitcnt lgkmcnt(0)
	v_mfma_scale_f32_16x16x128_f8f6f4 v[172:175], v[0:7], v[40:47], v[172:175], v204, v203 op_sel_hi:[0,0,0]
	v_mfma_scale_f32_16x16x128_f8f6f4 v[168:171], v[8:15], v[40:47], v[168:171], v204, v203 op_sel_hi:[0,0,0]
	v_mfma_scale_f32_16x16x128_f8f6f4 v[164:167], v[0:7], v[32:39], v[164:167], v204, v203 op_sel_hi:[0,0,0]
	v_mfma_scale_f32_16x16x128_f8f6f4 v[160:163], v[8:15], v[32:39], v[160:163], v204, v203 op_sel_hi:[0,0,0]
	v_mfma_scale_f32_16x16x128_f8f6f4 v[208:211], v[0:7], v[24:31], v[156:159], v204, v203 op_sel_hi:[0,0,0]
	v_mfma_scale_f32_16x16x128_f8f6f4 v[212:215], v[8:15], v[24:31], v[152:155], v204, v203 op_sel_hi:[0,0,0]
	v_mfma_scale_f32_16x16x128_f8f6f4 v[220:223], v[0:7], v[16:23], v[148:151], v204, v203 op_sel_hi:[0,0,0]
	v_mfma_scale_f32_16x16x128_f8f6f4 v[224:227], v[8:15], v[16:23], v[144:147], v204, v203 op_sel_hi:[0,0,0]
	s_setprio 0
	s_barrier
	s_mov_b32 m0, s46
	v_lshl_add_u64 v[216:217], s[28:29], 0, v[176:177]
	s_nop 2
	ds_read_b128 v[144:147], v205 offset:16384
	ds_read_b128 v[148:151], v205 offset:17408
	ds_read_b128 v[152:155], v205 offset:18432
	ds_read_b128 v[156:159], v205 offset:19456
	global_load_lds_dwordx4 v[216:217], off
	v_lshl_add_u64 v[216:217], s[28:29], 0, v[180:181]
	s_mov_b32 m0, s47
	s_nop 0
	global_load_lds_dwordx4 v[216:217], off
	s_barrier
	s_waitcnt lgkmcnt(0)
	s_setprio 1
	s_waitcnt lgkmcnt(0)
	v_mfma_scale_f32_16x16x128_f8f6f4 v[140:143], v[144:151], v[40:47], v[140:143], v204, v203 op_sel_hi:[0,0,0]
	v_mfma_scale_f32_16x16x128_f8f6f4 v[136:139], v[152:159], v[40:47], v[136:139], v204, v203 op_sel_hi:[0,0,0]
	v_mfma_scale_f32_16x16x128_f8f6f4 v[132:135], v[144:151], v[32:39], v[132:135], v204, v203 op_sel_hi:[0,0,0]
	v_mfma_scale_f32_16x16x128_f8f6f4 v[128:131], v[152:159], v[32:39], v[128:131], v204, v203 op_sel_hi:[0,0,0]
	v_mfma_scale_f32_16x16x128_f8f6f4 v[124:127], v[144:151], v[24:31], v[124:127], v204, v203 op_sel_hi:[0,0,0]
	v_mfma_scale_f32_16x16x128_f8f6f4 v[120:123], v[152:159], v[24:31], v[120:123], v204, v203 op_sel_hi:[0,0,0]
	v_mfma_scale_f32_16x16x128_f8f6f4 v[116:119], v[144:151], v[16:23], v[116:119], v204, v203 op_sel_hi:[0,0,0]
	v_mfma_scale_f32_16x16x128_f8f6f4 v[112:115], v[152:159], v[16:23], v[112:115], v204, v203 op_sel_hi:[0,0,0]
	s_setprio 0
	s_mov_b32 m0, s48
	v_add_u32_e32 v44, s79, v202
	s_barrier
	ds_read_b128 v[16:19], v44
	ds_read_b128 v[20:23], v44 offset:1024
	ds_read_b128 v[24:27], v44 offset:2048
	ds_read_b128 v[28:31], v44 offset:3072
	ds_read_b128 v[32:35], v44 offset:4096
	ds_read_b128 v[36:39], v44 offset:5120
	ds_read_b128 v[40:43], v44 offset:6144
	ds_read_b128 v[44:47], v44 offset:7168
	global_load_lds_dwordx4 v182, s[34:35]
	s_mov_b32 m0, s49
	v_mov_b32_e32 v185, v183
	global_load_lds_dwordx4 v184, s[34:35]
	s_barrier
	s_waitcnt lgkmcnt(0)
	v_lshl_add_u64 v[216:217], s[34:35], 0, v[182:183]
	v_lshl_add_u64 v[236:237], s[34:35], 0, v[184:185]
	s_setprio 1
	s_waitcnt lgkmcnt(0)
	v_mfma_scale_f32_16x16x128_f8f6f4 v[108:111], v[0:7], v[16:23], v[108:111], v204, v203 op_sel_hi:[0,0,0]
	v_mfma_scale_f32_16x16x128_f8f6f4 v[104:107], v[8:15], v[16:23], v[104:107], v204, v203 op_sel_hi:[0,0,0]
	v_mfma_scale_f32_16x16x128_f8f6f4 v[100:103], v[0:7], v[24:31], v[100:103], v204, v203 op_sel_hi:[0,0,0]
	v_mfma_scale_f32_16x16x128_f8f6f4 v[96:99], v[8:15], v[24:31], v[96:99], v204, v203 op_sel_hi:[0,0,0]
	v_mfma_scale_f32_16x16x128_f8f6f4 v[92:95], v[0:7], v[32:39], v[92:95], v204, v203 op_sel_hi:[0,0,0]
	v_mfma_scale_f32_16x16x128_f8f6f4 v[88:91], v[8:15], v[32:39], v[88:91], v204, v203 op_sel_hi:[0,0,0]
	v_mfma_scale_f32_16x16x128_f8f6f4 v[84:87], v[0:7], v[40:47], v[84:87], v204, v203 op_sel_hi:[0,0,0]
	v_mfma_scale_f32_16x16x128_f8f6f4 v[80:83], v[8:15], v[40:47], v[80:83], v204, v203 op_sel_hi:[0,0,0]
	s_setprio 0
	s_barrier
	s_add_u32 vcc_lo, s28, 0x400000
	s_addc_u32 vcc_hi, s29, 0
	s_mov_b32 m0, s50
	v_lshl_add_u64 v[0:1], vcc, 0, v[176:177]
	global_load_lds_dwordx4 v[0:1], off
	v_lshl_add_u64 v[0:1], vcc, 0, v[180:181]
	s_mov_b32 m0, s51
	s_nop 0
	global_load_lds_dwordx4 v[0:1], off
	s_waitcnt vmcnt(6)
	s_barrier
	s_setprio 1
	s_nop 0
	v_mfma_scale_f32_16x16x128_f8f6f4 v[76:79], v[144:151], v[16:23], v[76:79], v204, v203 op_sel_hi:[0,0,0]
	v_mfma_scale_f32_16x16x128_f8f6f4 v[72:75], v[152:159], v[16:23], v[72:75], v204, v203 op_sel_hi:[0,0,0]
	v_mfma_scale_f32_16x16x128_f8f6f4 v[68:71], v[144:151], v[24:31], v[68:71], v204, v203 op_sel_hi:[0,0,0]
	v_mfma_scale_f32_16x16x128_f8f6f4 v[64:67], v[152:159], v[24:31], v[64:67], v204, v203 op_sel_hi:[0,0,0]
	v_mfma_scale_f32_16x16x128_f8f6f4 v[60:63], v[144:151], v[32:39], v[60:63], v204, v203 op_sel_hi:[0,0,0]
	v_mfma_scale_f32_16x16x128_f8f6f4 v[56:59], v[152:159], v[32:39], v[56:59], v204, v203 op_sel_hi:[0,0,0]
	v_mfma_scale_f32_16x16x128_f8f6f4 v[228:231], v[144:151], v[40:47], v[52:55], v204, v203 op_sel_hi:[0,0,0]
	v_mfma_scale_f32_16x16x128_f8f6f4 v[232:235], v[152:159], v[40:47], v[48:51], v204, v203 op_sel_hi:[0,0,0]
	s_setprio 0
	s_barrier
	ds_read_b128 v[0:3], v205 offset:32768
	ds_read_b128 v[4:7], v205 offset:33792
	ds_read_b128 v[8:11], v205 offset:34816
	ds_read_b128 v[12:15], v205 offset:35840
	s_add_i32 vcc_lo, s79, s9
	v_add_u32_e32 v44, s77, v202
	v_lshl_add_u64 v[48:49], s[34:35], 0, v[196:197]
	s_mov_b32 m0, vcc_lo
	ds_read_b128 v[16:19], v44
	ds_read_b128 v[20:23], v44 offset:1024
	ds_read_b128 v[24:27], v44 offset:2048
	ds_read_b128 v[28:31], v44 offset:3072
	ds_read_b128 v[32:35], v44 offset:4096
	ds_read_b128 v[36:39], v44 offset:5120
	ds_read_b128 v[40:43], v44 offset:6144
	ds_read_b128 v[44:47], v44 offset:7168
	global_load_lds_dwordx4 v[48:49], off
	v_lshl_add_u64 v[48:49], s[34:35], 0, v[190:191]
	s_add_i32 m0, vcc_lo, 0x2000
	s_nop 0
	global_load_lds_dwordx4 v[48:49], off
	s_waitcnt lgkmcnt(8)
	s_barrier
	s_waitcnt lgkmcnt(0)
	s_setprio 1
	s_waitcnt lgkmcnt(0)
	s_nop 0
	v_mfma_scale_f32_16x16x128_f8f6f4 v[172:175], v[0:7], v[16:23], v[172:175], v204, v203 op_sel_hi:[0,0,0]
	v_mfma_scale_f32_16x16x128_f8f6f4 v[168:171], v[8:15], v[16:23], v[168:171], v204, v203 op_sel_hi:[0,0,0]
	v_mfma_scale_f32_16x16x128_f8f6f4 v[164:167], v[0:7], v[24:31], v[164:167], v204, v203 op_sel_hi:[0,0,0]
	v_mfma_scale_f32_16x16x128_f8f6f4 v[160:163], v[8:15], v[24:31], v[160:163], v204, v203 op_sel_hi:[0,0,0]
	v_mfma_scale_f32_16x16x128_f8f6f4 v[156:159], v[0:7], v[32:39], v[208:211], v204, v203 op_sel_hi:[0,0,0]
	v_mfma_scale_f32_16x16x128_f8f6f4 v[152:155], v[8:15], v[32:39], v[212:215], v204, v203 op_sel_hi:[0,0,0]
	v_mfma_scale_f32_16x16x128_f8f6f4 v[148:151], v[0:7], v[40:47], v[220:223], v204, v203 op_sel_hi:[0,0,0]
	v_mfma_scale_f32_16x16x128_f8f6f4 v[144:147], v[8:15], v[40:47], v[224:227], v204, v203 op_sel_hi:[0,0,0]
	s_setprio 0
	s_barrier
	s_mov_b32 m0, s53
	v_lshl_add_u64 v[196:197], s[30:31], 0, v[176:177]
	ds_read_b128 v[48:51], v205 offset:49152
	ds_read_b128 v[52:55], v205 offset:50176
	ds_read_b128 v[208:211], v205 offset:51200
	ds_read_b128 v[212:215], v205 offset:52224
	global_load_lds_dwordx4 v[196:197], off
	v_lshl_add_u64 v[196:197], s[30:31], 0, v[180:181]
	s_mov_b32 m0, s54
	s_nop 0
	global_load_lds_dwordx4 v[196:197], off
	s_barrier
	s_waitcnt lgkmcnt(0)
	s_setprio 1
	s_waitcnt lgkmcnt(0)
	s_nop 0
	v_mfma_scale_f32_16x16x128_f8f6f4 v[140:143], v[48:55], v[16:23], v[140:143], v204, v203 op_sel_hi:[0,0,0]
	v_mfma_scale_f32_16x16x128_f8f6f4 v[136:139], v[208:215], v[16:23], v[136:139], v204, v203 op_sel_hi:[0,0,0]
	v_mfma_scale_f32_16x16x128_f8f6f4 v[132:135], v[48:55], v[24:31], v[132:135], v204, v203 op_sel_hi:[0,0,0]
	v_mfma_scale_f32_16x16x128_f8f6f4 v[128:131], v[208:215], v[24:31], v[128:131], v204, v203 op_sel_hi:[0,0,0]
	v_mfma_scale_f32_16x16x128_f8f6f4 v[124:127], v[48:55], v[32:39], v[124:127], v204, v203 op_sel_hi:[0,0,0]
	v_mfma_scale_f32_16x16x128_f8f6f4 v[120:123], v[208:215], v[32:39], v[120:123], v204, v203 op_sel_hi:[0,0,0]
	v_mfma_scale_f32_16x16x128_f8f6f4 v[116:119], v[48:55], v[40:47], v[116:119], v204, v203 op_sel_hi:[0,0,0]
	v_mfma_scale_f32_16x16x128_f8f6f4 v[112:115], v[208:215], v[40:47], v[112:115], v204, v203 op_sel_hi:[0,0,0]
	s_setprio 0
	s_add_i32 s30, s77, s9
	v_add_u32_e32 v44, 0x1c000, v195
	v_lshl_add_u64 v[196:197], v[216:217], 0, s[16:17]
	s_mov_b32 m0, s30
	s_barrier
	ds_read_b128 v[16:19], v44
	ds_read_b128 v[20:23], v44 offset:1024
	ds_read_b128 v[24:27], v44 offset:2048
	ds_read_b128 v[28:31], v44 offset:3072
	ds_read_b128 v[32:35], v44 offset:4096
	ds_read_b128 v[36:39], v44 offset:5120
	ds_read_b128 v[40:43], v44 offset:6144
	ds_read_b128 v[44:47], v44 offset:7168
	global_load_lds_dwordx4 v[196:197], off
	v_lshl_add_u64 v[196:197], v[236:237], 0, s[16:17]
	s_add_i32 m0, s30, 0x2000
	s_nop 0
	global_load_lds_dwordx4 v[196:197], off
	s_barrier
	s_waitcnt lgkmcnt(0)
	s_setprio 1
	s_waitcnt lgkmcnt(0)
	s_nop 0
	v_mfma_scale_f32_16x16x128_f8f6f4 v[108:111], v[0:7], v[16:23], v[108:111], v204, v203 op_sel_hi:[0,0,0]
	v_mfma_scale_f32_16x16x128_f8f6f4 v[104:107], v[8:15], v[16:23], v[104:107], v204, v203 op_sel_hi:[0,0,0]
	v_mfma_scale_f32_16x16x128_f8f6f4 v[100:103], v[0:7], v[24:31], v[100:103], v204, v203 op_sel_hi:[0,0,0]
	v_mfma_scale_f32_16x16x128_f8f6f4 v[96:99], v[8:15], v[24:31], v[96:99], v204, v203 op_sel_hi:[0,0,0]
	v_mfma_scale_f32_16x16x128_f8f6f4 v[92:95], v[0:7], v[32:39], v[92:95], v204, v203 op_sel_hi:[0,0,0]
	v_mfma_scale_f32_16x16x128_f8f6f4 v[88:91], v[8:15], v[32:39], v[88:91], v204, v203 op_sel_hi:[0,0,0]
	v_mfma_scale_f32_16x16x128_f8f6f4 v[84:87], v[0:7], v[40:47], v[84:87], v204, v203 op_sel_hi:[0,0,0]
	v_mfma_scale_f32_16x16x128_f8f6f4 v[80:83], v[8:15], v[40:47], v[80:83], v204, v203 op_sel_hi:[0,0,0]
	s_setprio 0
	s_barrier
	s_add_u32 s28, s28, 0x404000
	s_addc_u32 s29, s29, 0
	s_mov_b32 m0, s55
	v_lshl_add_u64 v[0:1], s[28:29], 0, v[176:177]
	global_load_lds_dwordx4 v[0:1], off
	v_lshl_add_u64 v[0:1], s[28:29], 0, v[180:181]
	s_mov_b32 m0, s56
	s_nop 0
	global_load_lds_dwordx4 v[0:1], off
	s_waitcnt vmcnt(6)
	s_barrier
	s_setprio 1
	s_nop 0
	v_mfma_scale_f32_16x16x128_f8f6f4 v[76:79], v[48:55], v[16:23], v[76:79], v204, v203 op_sel_hi:[0,0,0]
	v_mfma_scale_f32_16x16x128_f8f6f4 v[72:75], v[208:215], v[16:23], v[72:75], v204, v203 op_sel_hi:[0,0,0]
	v_mfma_scale_f32_16x16x128_f8f6f4 v[68:71], v[48:55], v[24:31], v[68:71], v204, v203 op_sel_hi:[0,0,0]
	v_mfma_scale_f32_16x16x128_f8f6f4 v[64:67], v[208:215], v[24:31], v[64:67], v204, v203 op_sel_hi:[0,0,0]
	v_mfma_scale_f32_16x16x128_f8f6f4 v[60:63], v[48:55], v[32:39], v[60:63], v204, v203 op_sel_hi:[0,0,0]
	v_mfma_scale_f32_16x16x128_f8f6f4 v[56:59], v[208:215], v[32:39], v[56:59], v204, v203 op_sel_hi:[0,0,0]
	v_mfma_scale_f32_16x16x128_f8f6f4 v[52:55], v[48:55], v[40:47], v[228:231], v204, v203 op_sel_hi:[0,0,0]
	v_mfma_scale_f32_16x16x128_f8f6f4 v[48:51], v[208:215], v[40:47], v[232:235], v204, v203 op_sel_hi:[0,0,0]
	s_setprio 0
	s_add_i32 s78, s78, 2
	s_add_u32 s11, s11, 0x8000
	s_addc_u32 s23, s23, 0
	s_add_u32 s26, s26, 0x100
	s_addc_u32 s27, s27, 0
	s_cmp_gt_u32 s78, 13
	s_barrier
	s_cbranch_scc1 .LBB0_827

.LBB0_1044:
	s_add_u32 s34, s26, 0xf0e64000
	s_addc_u32 s35, s27, -1
	s_and_b64 s[30:31], s[28:29], exec
	s_cselect_b32 s31, 0, s34
	s_cselect_b32 s30, 0, s35
	s_add_u32 s36, s12, s31
	s_addc_u32 s37, s13, s30
	s_add_u32 s30, s8, s26
	s_addc_u32 s31, s9, s27
	s_add_u32 s30, s30, 0xf0e64000
	s_addc_u32 s31, s31, -1
	s_and_b64 s[28:29], s[28:29], exec
	s_cselect_b32 s29, s23, s31
	s_cselect_b32 s28, s22, s30
	s_add_u32 s30, s36, 0x4000
	s_waitcnt lgkmcnt(8)
	s_barrier
	s_waitcnt lgkmcnt(0)
	s_addc_u32 s31, s37, 0
	s_add_u32 s34, s28, 0x4000
	v_mov_b32_e32 v189, v183
	s_addc_u32 s35, s29, 0
	s_setprio 1
	s_waitcnt lgkmcnt(0)
	v_mfma_scale_f32_16x16x128_f8f6f4 v[172:175], v[0:7], v[40:47], v[172:175], v197, v196 op_sel_hi:[0,0,0]
	v_mfma_scale_f32_16x16x128_f8f6f4 v[168:171], v[8:15], v[40:47], v[168:171], v197, v196 op_sel_hi:[0,0,0]
	v_mfma_scale_f32_16x16x128_f8f6f4 v[164:167], v[0:7], v[32:39], v[164:167], v197, v196 op_sel_hi:[0,0,0]
	v_mfma_scale_f32_16x16x128_f8f6f4 v[160:163], v[8:15], v[32:39], v[160:163], v197, v196 op_sel_hi:[0,0,0]
	v_mfma_scale_f32_16x16x128_f8f6f4 v[202:205], v[0:7], v[24:31], v[156:159], v197, v196 op_sel_hi:[0,0,0]
	v_mfma_scale_f32_16x16x128_f8f6f4 v[206:209], v[8:15], v[24:31], v[152:155], v197, v196 op_sel_hi:[0,0,0]
	v_mfma_scale_f32_16x16x128_f8f6f4 v[210:213], v[0:7], v[16:23], v[148:151], v197, v196 op_sel_hi:[0,0,0]
	v_mfma_scale_f32_16x16x128_f8f6f4 v[214:217], v[8:15], v[16:23], v[144:147], v197, v196 op_sel_hi:[0,0,0]
	s_setprio 0
	s_barrier
	s_mov_b32 m0, s46
	v_lshl_add_u64 v[218:219], s[28:29], 0, v[176:177]
	s_nop 2
	ds_read_b128 v[144:147], v199 offset:16384
	ds_read_b128 v[148:151], v199 offset:17408
	ds_read_b128 v[152:155], v199 offset:18432
	ds_read_b128 v[156:159], v199 offset:19456
	global_load_lds_dwordx4 v[218:219], off
	v_lshl_add_u64 v[218:219], s[28:29], 0, v[180:181]
	s_mov_b32 m0, s47
	s_nop 0
	global_load_lds_dwordx4 v[218:219], off
	s_barrier
	s_waitcnt lgkmcnt(0)
	s_setprio 1
	s_waitcnt lgkmcnt(0)
	v_mfma_scale_f32_16x16x128_f8f6f4 v[140:143], v[144:151], v[40:47], v[140:143], v197, v196 op_sel_hi:[0,0,0]
	v_mfma_scale_f32_16x16x128_f8f6f4 v[136:139], v[152:159], v[40:47], v[136:139], v197, v196 op_sel_hi:[0,0,0]
	v_mfma_scale_f32_16x16x128_f8f6f4 v[132:135], v[144:151], v[32:39], v[132:135], v197, v196 op_sel_hi:[0,0,0]
	v_mfma_scale_f32_16x16x128_f8f6f4 v[128:131], v[152:159], v[32:39], v[128:131], v197, v196 op_sel_hi:[0,0,0]
	v_mfma_scale_f32_16x16x128_f8f6f4 v[124:127], v[144:151], v[24:31], v[124:127], v197, v196 op_sel_hi:[0,0,0]
	v_mfma_scale_f32_16x16x128_f8f6f4 v[120:123], v[152:159], v[24:31], v[120:123], v197, v196 op_sel_hi:[0,0,0]
	v_mfma_scale_f32_16x16x128_f8f6f4 v[116:119], v[144:151], v[16:23], v[116:119], v197, v196 op_sel_hi:[0,0,0]
	v_mfma_scale_f32_16x16x128_f8f6f4 v[112:115], v[152:159], v[16:23], v[112:115], v197, v196 op_sel_hi:[0,0,0]
	s_setprio 0
	v_add_u32_e32 v44, s76, v194
	s_mov_b32 m0, s48
	s_barrier
	ds_read_b128 v[16:19], v44
	ds_read_b128 v[20:23], v44 offset:1024
	ds_read_b128 v[24:27], v44 offset:2048
	ds_read_b128 v[28:31], v44 offset:3072
	ds_read_b128 v[32:35], v44 offset:4096
	ds_read_b128 v[36:39], v44 offset:5120
	ds_read_b128 v[40:43], v44 offset:6144
	ds_read_b128 v[44:47], v44 offset:7168
	global_load_lds_dwordx4 v184, s[36:37]
	s_mov_b32 m0, s49
	s_nop 0
	global_load_lds_dwordx4 v186, s[36:37]
	s_barrier
	s_waitcnt lgkmcnt(0)
	s_setprio 1
	s_waitcnt lgkmcnt(0)
	v_mfma_scale_f32_16x16x128_f8f6f4 v[108:111], v[0:7], v[16:23], v[108:111], v197, v196 op_sel_hi:[0,0,0]
	v_mfma_scale_f32_16x16x128_f8f6f4 v[104:107], v[8:15], v[16:23], v[104:107], v197, v196 op_sel_hi:[0,0,0]
	v_mfma_scale_f32_16x16x128_f8f6f4 v[100:103], v[0:7], v[24:31], v[100:103], v197, v196 op_sel_hi:[0,0,0]
	v_mfma_scale_f32_16x16x128_f8f6f4 v[96:99], v[8:15], v[24:31], v[96:99], v197, v196 op_sel_hi:[0,0,0]
	v_mfma_scale_f32_16x16x128_f8f6f4 v[92:95], v[0:7], v[32:39], v[92:95], v197, v196 op_sel_hi:[0,0,0]
	v_mfma_scale_f32_16x16x128_f8f6f4 v[88:91], v[8:15], v[32:39], v[88:91], v197, v196 op_sel_hi:[0,0,0]
	v_mfma_scale_f32_16x16x128_f8f6f4 v[84:87], v[0:7], v[40:47], v[84:87], v197, v196 op_sel_hi:[0,0,0]
	v_mfma_scale_f32_16x16x128_f8f6f4 v[80:83], v[8:15], v[40:47], v[80:83], v197, v196 op_sel_hi:[0,0,0]
	s_setprio 0
	s_barrier
	s_add_u32 vcc_lo, s28, 0x1000
	s_addc_u32 vcc_hi, s29, 0
	s_mov_b32 m0, s50
	v_lshl_add_u64 v[0:1], vcc, 0, v[176:177]
	global_load_lds_dwordx4 v[0:1], off
	v_lshl_add_u64 v[0:1], vcc, 0, v[180:181]
	s_mov_b32 m0, s51
	s_nop 0
	global_load_lds_dwordx4 v[0:1], off
	s_waitcnt vmcnt(6)
	s_barrier
	s_setprio 1
	s_nop 0
	v_mfma_scale_f32_16x16x128_f8f6f4 v[76:79], v[144:151], v[16:23], v[76:79], v197, v196 op_sel_hi:[0,0,0]
	v_mfma_scale_f32_16x16x128_f8f6f4 v[72:75], v[152:159], v[16:23], v[72:75], v197, v196 op_sel_hi:[0,0,0]
	v_mfma_scale_f32_16x16x128_f8f6f4 v[68:71], v[144:151], v[24:31], v[68:71], v197, v196 op_sel_hi:[0,0,0]
	v_mfma_scale_f32_16x16x128_f8f6f4 v[64:67], v[152:159], v[24:31], v[64:67], v197, v196 op_sel_hi:[0,0,0]
	v_mfma_scale_f32_16x16x128_f8f6f4 v[60:63], v[144:151], v[32:39], v[60:63], v197, v196 op_sel_hi:[0,0,0]
	v_mfma_scale_f32_16x16x128_f8f6f4 v[56:59], v[152:159], v[32:39], v[56:59], v197, v196 op_sel_hi:[0,0,0]
	v_mfma_scale_f32_16x16x128_f8f6f4 v[218:221], v[144:151], v[40:47], v[52:55], v197, v196 op_sel_hi:[0,0,0]
	v_mfma_scale_f32_16x16x128_f8f6f4 v[222:225], v[152:159], v[40:47], v[48:51], v197, v196 op_sel_hi:[0,0,0]
	s_setprio 0
	s_barrier
	ds_read_b128 v[0:3], v199 offset:32768
	ds_read_b128 v[4:7], v199 offset:33792
	ds_read_b128 v[8:11], v199 offset:34816
	ds_read_b128 v[12:15], v199 offset:35840
	s_add_i32 vcc_lo, s76, s45
	v_add_u32_e32 v44, s78, v194
	v_lshl_add_u64 v[48:49], s[36:37], 0, v[182:183]
	s_mov_b32 m0, vcc_lo
	ds_read_b128 v[16:19], v44
	ds_read_b128 v[20:23], v44 offset:1024
	ds_read_b128 v[24:27], v44 offset:2048
	ds_read_b128 v[28:31], v44 offset:3072
	ds_read_b128 v[32:35], v44 offset:4096
	ds_read_b128 v[36:39], v44 offset:5120
	ds_read_b128 v[40:43], v44 offset:6144
	ds_read_b128 v[44:47], v44 offset:7168
	global_load_lds_dwordx4 v[48:49], off
	v_lshl_add_u64 v[48:49], s[36:37], 0, v[188:189]
	s_add_i32 m0, vcc_lo, 0x2000
	s_nop 0
	global_load_lds_dwordx4 v[48:49], off
	s_waitcnt lgkmcnt(8)
	s_barrier
	s_waitcnt lgkmcnt(0)
	s_setprio 1
	s_waitcnt lgkmcnt(0)
	s_nop 0
	v_mfma_scale_f32_16x16x128_f8f6f4 v[172:175], v[0:7], v[16:23], v[172:175], v197, v196 op_sel_hi:[0,0,0]
	v_mfma_scale_f32_16x16x128_f8f6f4 v[168:171], v[8:15], v[16:23], v[168:171], v197, v196 op_sel_hi:[0,0,0]
	v_mfma_scale_f32_16x16x128_f8f6f4 v[164:167], v[0:7], v[24:31], v[164:167], v197, v196 op_sel_hi:[0,0,0]
	v_mfma_scale_f32_16x16x128_f8f6f4 v[160:163], v[8:15], v[24:31], v[160:163], v197, v196 op_sel_hi:[0,0,0]
	v_mfma_scale_f32_16x16x128_f8f6f4 v[156:159], v[0:7], v[32:39], v[202:205], v197, v196 op_sel_hi:[0,0,0]
	v_mfma_scale_f32_16x16x128_f8f6f4 v[152:155], v[8:15], v[32:39], v[206:209], v197, v196 op_sel_hi:[0,0,0]
	v_mfma_scale_f32_16x16x128_f8f6f4 v[148:151], v[0:7], v[40:47], v[210:213], v197, v196 op_sel_hi:[0,0,0]
	v_mfma_scale_f32_16x16x128_f8f6f4 v[144:147], v[8:15], v[40:47], v[214:217], v197, v196 op_sel_hi:[0,0,0]
	s_setprio 0
	s_barrier
	s_mov_b32 m0, s52
	s_nop 2
	v_lshl_add_u64 v[210:211], s[34:35], 0, v[176:177]
	ds_read_b128 v[48:51], v199 offset:49152
	ds_read_b128 v[52:55], v199 offset:50176
	ds_read_b128 v[202:205], v199 offset:51200
	ds_read_b128 v[206:209], v199 offset:52224
	global_load_lds_dwordx4 v[210:211], off
	v_lshl_add_u64 v[210:211], s[34:35], 0, v[180:181]
	s_mov_b32 m0, s53
	s_nop 0
	global_load_lds_dwordx4 v[210:211], off
	s_barrier
	s_waitcnt lgkmcnt(0)
	s_setprio 1
	s_waitcnt lgkmcnt(0)
	v_mfma_scale_f32_16x16x128_f8f6f4 v[140:143], v[48:55], v[16:23], v[140:143], v197, v196 op_sel_hi:[0,0,0]
	v_mfma_scale_f32_16x16x128_f8f6f4 v[136:139], v[202:209], v[16:23], v[136:139], v197, v196 op_sel_hi:[0,0,0]
	v_mfma_scale_f32_16x16x128_f8f6f4 v[132:135], v[48:55], v[24:31], v[132:135], v197, v196 op_sel_hi:[0,0,0]
	v_mfma_scale_f32_16x16x128_f8f6f4 v[128:131], v[202:209], v[24:31], v[128:131], v197, v196 op_sel_hi:[0,0,0]
	v_mfma_scale_f32_16x16x128_f8f6f4 v[124:127], v[48:55], v[32:39], v[124:127], v197, v196 op_sel_hi:[0,0,0]
	v_mfma_scale_f32_16x16x128_f8f6f4 v[120:123], v[202:209], v[32:39], v[120:123], v197, v196 op_sel_hi:[0,0,0]
	v_mfma_scale_f32_16x16x128_f8f6f4 v[116:119], v[48:55], v[40:47], v[116:119], v197, v196 op_sel_hi:[0,0,0]
	v_mfma_scale_f32_16x16x128_f8f6f4 v[112:115], v[202:209], v[40:47], v[112:115], v197, v196 op_sel_hi:[0,0,0]
	s_setprio 0
	s_add_i32 s34, s78, s45
	v_add_u32_e32 v44, 0x1c000, v201
	s_mov_b32 m0, s34
	s_barrier
	ds_read_b128 v[16:19], v44
	ds_read_b128 v[20:23], v44 offset:1024
	ds_read_b128 v[24:27], v44 offset:2048
	ds_read_b128 v[28:31], v44 offset:3072
	ds_read_b128 v[32:35], v44 offset:4096
	ds_read_b128 v[36:39], v44 offset:5120
	ds_read_b128 v[40:43], v44 offset:6144
	ds_read_b128 v[44:47], v44 offset:7168
	global_load_lds_dwordx4 v184, s[30:31]
	s_add_i32 m0, s34, 0x2000
	s_nop 0
	global_load_lds_dwordx4 v186, s[30:31]
	s_barrier
	s_waitcnt lgkmcnt(0)
	s_setprio 1
	s_waitcnt lgkmcnt(0)
	s_nop 0
	v_mfma_scale_f32_16x16x128_f8f6f4 v[108:111], v[0:7], v[16:23], v[108:111], v197, v196 op_sel_hi:[0,0,0]
	v_mfma_scale_f32_16x16x128_f8f6f4 v[104:107], v[8:15], v[16:23], v[104:107], v197, v196 op_sel_hi:[0,0,0]
	v_mfma_scale_f32_16x16x128_f8f6f4 v[100:103], v[0:7], v[24:31], v[100:103], v197, v196 op_sel_hi:[0,0,0]
	v_mfma_scale_f32_16x16x128_f8f6f4 v[96:99], v[8:15], v[24:31], v[96:99], v197, v196 op_sel_hi:[0,0,0]
	v_mfma_scale_f32_16x16x128_f8f6f4 v[92:95], v[0:7], v[32:39], v[92:95], v197, v196 op_sel_hi:[0,0,0]
	v_mfma_scale_f32_16x16x128_f8f6f4 v[88:91], v[8:15], v[32:39], v[88:91], v197, v196 op_sel_hi:[0,0,0]
	v_mfma_scale_f32_16x16x128_f8f6f4 v[84:87], v[0:7], v[40:47], v[84:87], v197, v196 op_sel_hi:[0,0,0]
	v_mfma_scale_f32_16x16x128_f8f6f4 v[80:83], v[8:15], v[40:47], v[80:83], v197, v196 op_sel_hi:[0,0,0]
	s_setprio 0
	s_barrier
	s_add_u32 s28, s28, 0x5000
	s_addc_u32 s29, s29, 0
	s_mov_b32 m0, s54
	v_lshl_add_u64 v[0:1], s[28:29], 0, v[176:177]
	global_load_lds_dwordx4 v[0:1], off
	v_lshl_add_u64 v[0:1], s[28:29], 0, v[180:181]
	s_mov_b32 m0, s55
	s_nop 0
	global_load_lds_dwordx4 v[0:1], off
	s_waitcnt vmcnt(6)
	s_barrier
	s_setprio 1
	s_nop 0
	v_mfma_scale_f32_16x16x128_f8f6f4 v[76:79], v[48:55], v[16:23], v[76:79], v197, v196 op_sel_hi:[0,0,0]
	v_mfma_scale_f32_16x16x128_f8f6f4 v[72:75], v[202:209], v[16:23], v[72:75], v197, v196 op_sel_hi:[0,0,0]
	v_mfma_scale_f32_16x16x128_f8f6f4 v[68:71], v[48:55], v[24:31], v[68:71], v197, v196 op_sel_hi:[0,0,0]
	v_mfma_scale_f32_16x16x128_f8f6f4 v[64:67], v[202:209], v[24:31], v[64:67], v197, v196 op_sel_hi:[0,0,0]
	v_mfma_scale_f32_16x16x128_f8f6f4 v[60:63], v[48:55], v[32:39], v[60:63], v197, v196 op_sel_hi:[0,0,0]
	v_mfma_scale_f32_16x16x128_f8f6f4 v[56:59], v[202:209], v[32:39], v[56:59], v197, v196 op_sel_hi:[0,0,0]
	v_mfma_scale_f32_16x16x128_f8f6f4 v[52:55], v[48:55], v[40:47], v[218:221], v197, v196 op_sel_hi:[0,0,0]
	v_mfma_scale_f32_16x16x128_f8f6f4 v[48:51], v[202:209], v[40:47], v[222:225], v197, v196 op_sel_hi:[0,0,0]
	s_setprio 0
	s_add_i32 s83, s83, 2
	s_add_u32 s26, s26, 0x8000
	s_addc_u32 s27, s27, 0
	s_cmp_gt_u32 s83, 13
	s_barrier
	s_cbranch_scc1 .LBB0_1047
